# v21 + gate path staging of Wz/Wg: loads batched, full vmcnt(0) wait per ds_write group
# speedup vs baseline: 1.0051x; 1.0051x over previous
.LBB0_127:
	v_lshl_add_u64 v[10:11], v[2:3], 0, s[2:3]
	v_add_co_u32_e32 v6, vcc, 0xc000, v10
	s_add_u32 s2, s2, 0x60400
	s_nop 0
	v_addc_co_u32_e32 v7, vcc, 0, v11, vcc
	v_add_co_u32_e32 v8, vcc, 0x6000, v10
	s_addc_u32 s3, s3, 0
	s_nop 0
	v_addc_co_u32_e32 v9, vcc, 0, v11, vcc
	global_load_dword v226, v[6:7], off offset:64
	global_load_dword v227, v[8:9], off
	v_add_co_u32_e32 v8, vcc, 0x18000, v10
	s_cmp_lg_u32 s2, 0x181000
	s_nop 0
	v_addc_co_u32_e32 v9, vcc, 0, v11, vcc
	v_add_co_u32_e32 v12, vcc, 0x12000, v10
	s_nop 0
	v_addc_co_u32_e32 v13, vcc, 0, v11, vcc
	global_load_dword v228, v[8:9], off offset:192
	global_load_dword v229, v[12:13], off offset:128
	v_add_co_u32_e32 v8, vcc, 0x24000, v10
	s_nop 0
	v_addc_co_u32_e32 v9, vcc, 0, v11, vcc
	v_add_co_u32_e32 v12, vcc, 0x1e000, v10
	s_nop 1
	v_addc_co_u32_e32 v13, vcc, 0, v11, vcc
	global_load_dword v230, v[8:9], off offset:320
	s_nop 0
	global_load_dword v231, v[12:13], off offset:256
	v_add_co_u32_e32 v12, vcc, 0x30000, v10
	s_nop 0
	v_addc_co_u32_e32 v13, vcc, 0, v11, vcc
	v_add_co_u32_e32 v14, vcc, 0x2a000, v10
	s_nop 1
	v_addc_co_u32_e32 v15, vcc, 0, v11, vcc
	global_load_dword v232, v[12:13], off offset:448
	global_load_dword v233, v[14:15], off offset:384
	v_add_co_u32_e32 v12, vcc, 0x3c000, v10
	s_nop 0
	v_addc_co_u32_e32 v13, vcc, 0, v11, vcc
	v_add_co_u32_e32 v14, vcc, 0x36000, v10
	s_nop 1
	v_addc_co_u32_e32 v15, vcc, 0, v11, vcc
	global_load_dword v234, v[12:13], off offset:576
	global_load_dword v235, v[14:15], off offset:512
	v_add_co_u32_e32 v12, vcc, 0x48000, v10
	s_waitcnt vmcnt(0)
	v_cvt_pk_bf16_f32 v6, v227, v226
	v_cvt_pk_bf16_f32 v7, v229, v228
	v_cvt_pk_bf16_f32 v8, v231, v230
	v_cvt_pk_bf16_f32 v9, v233, v232
	ds_write_b128 v4, v[6:9]
	s_nop 0
	v_addc_co_u32_e32 v13, vcc, 0, v11, vcc
	v_add_co_u32_e32 v14, vcc, 0x42000, v10
	s_nop 0
	v_addc_co_u32_e32 v15, vcc, 0, v11, vcc
	global_load_dword v237, v[12:13], off offset:704
	global_load_dword v238, v[14:15], off offset:640
	v_add_co_u32_e32 v8, vcc, 0x54000, v10
	s_nop 0
	v_addc_co_u32_e32 v9, vcc, 0, v11, vcc
	v_add_co_u32_e32 v12, vcc, 0x4e000, v10
	s_nop 1
	v_addc_co_u32_e32 v13, vcc, 0, v11, vcc
	global_load_dword v239, v[8:9], off offset:832
	s_nop 0
	global_load_dword v240, v[12:13], off offset:768
	v_add_co_u32_e32 v12, vcc, 0x60000, v10
	s_nop 0
	v_addc_co_u32_e32 v13, vcc, 0, v11, vcc
	v_add_co_u32_e32 v10, vcc, 0x5a000, v10
	s_nop 1
	v_addc_co_u32_e32 v11, vcc, 0, v11, vcc
	global_load_dword v241, v[12:13], off offset:960
	global_load_dword v242, v[10:11], off offset:896
	s_waitcnt vmcnt(0)
	v_cvt_pk_bf16_f32 v6, v235, v234
	v_cvt_pk_bf16_f32 v7, v238, v237
	v_cvt_pk_bf16_f32 v8, v240, v239
	v_cvt_pk_bf16_f32 v9, v242, v241
	ds_write_b128 v4, v[6:9] offset:16
	v_add_u32_e32 v4, 32, v4
	s_cbranch_scc1 .LBB0_127
	v_mov_b32_e32 v2, 0
	v_lshlrev_b32_e32 v12, 2, v0
	v_mov_b32_e32 v13, v2
	v_lshl_add_u64 v[10:11], s[64:65], 0, v[12:13]
	v_add_co_u32_e32 v14, vcc, 0x1000, v10
	s_add_i32 s2, 0, 0x10100
	s_nop 0
	v_addc_co_u32_e32 v15, vcc, 0, v11, vcc
	global_load_dword v243, v[14:15], off
	global_load_dword v245, v12, s[64:65]
	v_add_co_u32_e32 v16, vcc, 0x3000, v10
	v_lshl_add_u32 v44, v0, 5, s2
	s_nop 0
	v_addc_co_u32_e32 v17, vcc, 0, v11, vcc
	v_add_co_u32_e32 v18, vcc, 0x2000, v10
	v_lshlrev_b32_e32 v67, 5, v130
	s_nop 0
	v_addc_co_u32_e32 v19, vcc, 0, v11, vcc
	v_add_co_u32_e32 v20, vcc, 0x5000, v10
	v_and_b32_e32 v66, 48, v0
	s_nop 0
	v_addc_co_u32_e32 v21, vcc, 0, v11, vcc
	v_add_co_u32_e32 v22, vcc, 0x4000, v10
	v_cmp_gt_u32_e64 s[4:5], 32, v236
	s_nop 0
	v_addc_co_u32_e32 v23, vcc, 0, v11, vcc
	v_add_co_u32_e32 v24, vcc, 0x7000, v10
	s_mov_b32 s3, 0
	s_nop 0
	v_addc_co_u32_e32 v25, vcc, 0, v11, vcc
	v_add_co_u32_e32 v26, vcc, 0x6000, v10
	v_add3_u32 v64, s2, v67, v66
	s_nop 0
	v_addc_co_u32_e32 v27, vcc, 0, v11, vcc
	v_add_co_u32_e32 v28, vcc, 0x9000, v10
	global_load_dword v246, v[16:17], off
	global_load_dword v247, v[18:19], off
	v_addc_co_u32_e32 v29, vcc, 0, v11, vcc
	v_add_co_u32_e32 v30, vcc, 0x8000, v10
	global_load_dword v248, v[20:21], off
	global_load_dword v249, v[22:23], off
	v_addc_co_u32_e32 v31, vcc, 0, v11, vcc
	v_add_co_u32_e32 v32, vcc, 0xb000, v10
	global_load_dword v250, v[24:25], off
	global_load_dword v251, v[26:27], off
	v_addc_co_u32_e32 v33, vcc, 0, v11, vcc
	v_add_co_u32_e32 v34, vcc, 0xa000, v10
	global_load_dword v252, v[28:29], off
	global_load_dword v253, v[30:31], off
	v_addc_co_u32_e32 v35, vcc, 0, v11, vcc
	v_add_co_u32_e32 v36, vcc, 0xd000, v10
	global_load_dword v226, v[32:33], off
	global_load_dword v227, v[34:35], off
	v_addc_co_u32_e32 v37, vcc, 0, v11, vcc
	v_add_co_u32_e32 v38, vcc, 0xc000, v10
	s_nop 0
	v_addc_co_u32_e32 v39, vcc, 0, v11, vcc
	global_load_dword v228, v[36:37], off
	global_load_dword v229, v[38:39], off
	v_add_co_u32_e32 v40, vcc, 0xf000, v10
	s_nop 1
	v_addc_co_u32_e32 v41, vcc, 0, v11, vcc
	v_add_co_u32_e32 v42, vcc, 0xe000, v10
	s_nop 0
	v_addc_co_u32_e32 v43, vcc, 0, v11, vcc
	global_load_dword v230, v[40:41], off
	global_load_dword v231, v[42:43], off
	global_load_dword v232, v[14:15], off offset:2048
	global_load_dword v233, v12, s[64:65] offset:2048
	s_waitcnt vmcnt(0)
	v_cvt_pk_bf16_f32 v4, v245, v243
	v_cvt_pk_bf16_f32 v5, v247, v246
	v_cvt_pk_bf16_f32 v6, v249, v248
	v_cvt_pk_bf16_f32 v7, v251, v250
	v_cvt_pk_bf16_f32 v8, v253, v252
	v_cvt_pk_bf16_f32 v9, v227, v226
	v_cvt_pk_bf16_f32 v10, v229, v228
	v_cvt_pk_bf16_f32 v11, v231, v230
	ds_write_b128 v44, v[4:7]
	ds_write_b128 v44, v[8:11] offset:16
	v_mov_b32_e32 v6, 0
	v_mov_b32_e32 v7, 0
	v_mov_b32_e32 v8, 0
	v_mov_b32_e32 v9, 0
	global_load_dword v234, v[16:17], off offset:2048
	global_load_dword v235, v[18:19], off offset:2048
	global_load_dword v237, v[20:21], off offset:2048
	global_load_dword v238, v[22:23], off offset:2048
	global_load_dword v239, v[24:25], off offset:2048
	global_load_dword v240, v[26:27], off offset:2048
	global_load_dword v241, v[28:29], off offset:2048
	global_load_dword v242, v[30:31], off offset:2048
	global_load_dword v243, v[32:33], off offset:2048
	global_load_dword v245, v[34:35], off offset:2048
	global_load_dword v246, v[36:37], off offset:2048
	global_load_dword v247, v[38:39], off offset:2048
	global_load_dword v248, v[40:41], off offset:2048
	global_load_dword v249, v[42:43], off offset:2048
	s_waitcnt vmcnt(0)
	v_cvt_pk_bf16_f32 v10, v233, v232
	v_cvt_pk_bf16_f32 v11, v235, v234
	v_cvt_pk_bf16_f32 v12, v238, v237
	v_cvt_pk_bf16_f32 v13, v240, v239
	v_cvt_pk_bf16_f32 v14, v242, v241
	v_cvt_pk_bf16_f32 v15, v245, v243
	v_cvt_pk_bf16_f32 v16, v247, v246
	v_cvt_pk_bf16_f32 v17, v249, v248
	ds_write_b128 v44, v[10:13] offset:16384
	ds_write_b128 v44, v[14:17] offset:16400
	s_waitcnt lgkmcnt(0)
	s_barrier
	s_and_saveexec_b64 s[6:7], s[4:5]
	v_lshl_add_u32 v3, s95, 12, v64
	ds_read_b128 v[6:9], v3
	s_or_b64 exec, exec, s[6:7]
	v_and_b32_e32 v4, 48, v236
	v_mov_b32_e32 v5, v2
	v_lshl_add_u64 v[62:63], s[66:67], 0, v[4:5]
	s_lshl_b32 s2, s95, 7
	v_lshl_add_u64 v[4:5], s[2:3], 2, v[62:63]
	global_load_dwordx4 v[10:13], v[4:5], off
	s_lshl_b32 s10, s95, 3
	s_or_b32 s8, s10, 1
	v_mov_b32_e32 v3, 0
	v_mov_b32_e32 v4, 0
	v_mov_b32_e32 v5, 0
	s_and_saveexec_b64 s[6:7], s[4:5]
	v_lshl_add_u32 v2, s8, 9, v64
	ds_read_b128 v[2:5], v2
	s_or_b64 exec, exec, s[6:7]
	s_lshl_b32 s6, s8, 4
	s_mov_b32 s7, s3
	v_lshl_add_u64 v[14:15], s[6:7], 2, v[62:63]
	global_load_dwordx4 v[14:17], v[14:15], off
	s_or_b32 s6, s10, 2
	s_mov_b32 s7, 0
	v_mov_b32_e32 v18, 0
	v_mov_b32_e32 v22, 0
	v_mov_b32_e32 v23, 0
	v_mov_b32_e32 v24, 0
	v_mov_b32_e32 v25, 0
	s_and_saveexec_b64 s[8:9], s[4:5]
	v_lshl_add_u32 v19, s6, 9, v64
	ds_read_b128 v[22:25], v19
	s_or_b64 exec, exec, s[8:9]
	s_lshl_b32 s6, s6, 4
	v_lshl_add_u64 v[20:21], s[6:7], 2, v[62:63]
	global_load_dwordx4 v[26:29], v[20:21], off
	s_or_b32 s6, s10, 3
	v_mov_b32_e32 v19, 0
	v_mov_b32_e32 v20, 0
	v_mov_b32_e32 v21, 0
	s_and_saveexec_b64 s[8:9], s[4:5]
	v_lshl_add_u32 v18, s6, 9, v64
	ds_read_b128 v[18:21], v18
	s_or_b64 exec, exec, s[8:9]
	s_lshl_b32 s6, s6, 4
	v_lshl_add_u64 v[30:31], s[6:7], 2, v[62:63]
	global_load_dwordx4 v[30:33], v[30:31], off
	s_or_b32 s6, s10, 4
	v_mov_b32_e32 v34, 0
	v_mov_b32_e32 v38, 0
	v_mov_b32_e32 v39, 0
	v_mov_b32_e32 v40, 0
	v_mov_b32_e32 v41, 0
	s_and_saveexec_b64 s[8:9], s[4:5]
	v_lshl_add_u32 v35, s6, 9, v64
	ds_read_b128 v[38:41], v35
	s_or_b64 exec, exec, s[8:9]
	s_lshl_b32 s6, s6, 4
	v_lshl_add_u64 v[36:37], s[6:7], 2, v[62:63]
	global_load_dwordx4 v[42:45], v[36:37], off
	s_or_b32 s6, s10, 5
	v_mov_b32_e32 v35, 0
	v_mov_b32_e32 v36, 0
	v_mov_b32_e32 v37, 0
	s_and_saveexec_b64 s[8:9], s[4:5]
	v_lshl_add_u32 v34, s6, 9, v64
	ds_read_b128 v[34:37], v34
	s_or_b64 exec, exec, s[8:9]
	s_lshl_b32 s6, s6, 4
	v_lshl_add_u64 v[46:47], s[6:7], 2, v[62:63]
	global_load_dwordx4 v[46:49], v[46:47], off
	s_or_b32 s6, s10, 6
	v_mov_b32_e32 v50, 0
	v_mov_b32_e32 v54, 0
	v_mov_b32_e32 v55, 0
	v_mov_b32_e32 v56, 0
	v_mov_b32_e32 v57, 0
	s_and_saveexec_b64 s[8:9], s[4:5]
	v_lshl_add_u32 v51, s6, 9, v64
	ds_read_b128 v[54:57], v51
	s_or_b64 exec, exec, s[8:9]
	s_lshl_b32 s6, s6, 4
	v_lshl_add_u64 v[52:53], s[6:7], 2, v[62:63]
	global_load_dwordx4 v[58:61], v[52:53], off
	s_or_b32 s8, s10, 7
	v_mov_b32_e32 v51, 0
	v_mov_b32_e32 v52, 0
	v_mov_b32_e32 v53, 0
	s_and_saveexec_b64 s[6:7], s[4:5]
	v_lshl_add_u32 v50, s8, 9, v64
	ds_read_b128 v[50:53], v50
	s_or_b64 exec, exec, s[6:7]
	v_readlane_b32 s6, v254, 0
	s_cmpk_lt_i32 s6, 0x100
	v_readlane_b32 s7, v254, 1
	s_cbranch_scc0 .LBB0_161
	s_lshl_b32 s24, s8, 4
	s_mov_b32 s25, 0
	v_lshl_add_u64 v[62:63], s[24:25], 2, v[62:63]
	global_load_dwordx4 v[62:65], v[62:63], off
	v_readlane_b32 s9, v254, 2
	s_lshr_b32 s6, s9, 8
	s_bfe_u32 s8, s9, 0x20006
	s_lshl_b32 s7, s6, 11
	v_lshrrev_b32_e32 v68, 4, v236
	s_lshl_b32 s28, s8, 4
	s_lshl_b32 s24, s6, 10
	s_add_i32 s7, s7, 0
	v_lshlrev_b32_e32 v70, 4, v68
	s_cmp_eq_u32 s6, 1
	v_add3_u32 v1, s7, v1, v70
	s_cselect_b64 s[6:7], -1, 0
	s_lshl_b32 s8, s8, 10
	s_add_i32 s31, 0, 0x18100
	s_add_i32 s29, s31, s8
	v_lshlrev_b32_e32 v69, 2, v68
	s_cmpk_lt_u32 s9, 0x100
	s_cselect_b64 s[8:9], -1, 0
	s_lshl_b32 s10, s95, 10
	v_lshlrev_b32_e32 v72, 2, v69
	v_mov_b32_e32 v73, 0
	v_readlane_b32 s26, v254, 0
	s_add_i32 s31, s31, s10
	s_add_i32 s12, 0, 0x19100
	v_or_b32_e32 v76, s28, v69
	v_lshl_add_u64 v[68:69], s[58:59], 0, v[72:73]
	s_mov_b64 s[10:11], 0x41680000
	v_readlane_b32 s27, v254, 1
	s_mov_b32 s72, s26
	s_ashr_i32 s73, s26, 31
	v_lshl_add_u32 v71, v130, 1, s12
	v_lshl_add_u64 v[74:75], v[68:69], 0, s[10:11]
	v_add3_u32 v72, s12, v67, v70
	s_or_b32 s10, s2, 16
	s_mov_b32 s11, s25
	s_or_b32 s12, s2, 32
	s_mov_b32 s13, s25
	s_or_b32 s14, s2, 48
	s_mov_b32 s15, s25
	s_or_b32 s16, s2, 64
	s_mov_b32 s17, s25
	s_or_b32 s18, s2, 0x50
	s_mov_b32 s19, s25
	s_or_b32 s20, s2, 0x60
	s_mov_b32 s21, s25
	s_or_b32 s22, s2, 0x70
	s_mov_b32 s23, s25
	s_lshl_b64 s[26:27], s[72:73], 18
	v_or_b32_e32 v67, s28, v130
	s_lshl_b64 s[24:25], s[24:25], 1
	v_lshlrev_b32_e32 v67, 12, v67
	s_add_u32 s24, s58, s24
	v_or3_b32 v66, s26, v67, v66
	v_mov_b32_e32 v67, s27
	s_addc_u32 s25, s59, s25
	s_mov_b32 s70, s72
	v_lshlrev_b32_e32 v68, 5, v76
	v_lshl_add_u64 v[66:67], s[24:25], 0, v[66:67]
	s_mov_b64 s[24:25], 0x31680100
	s_ashr_i32 s97, s96, 31
	v_writelane_b32 v254, s70, 0
	v_lshlrev_b32_e32 v84, 4, v236
	v_lshl_add_u64 v[76:77], v[66:67], 0, s[24:25]
	s_lshl_b64 s[24:25], s[96:97], 18
	s_mov_b64 s[26:27], 0x200
	v_add_u32_e32 v85, v71, v68
	s_mov_b32 s35, 0xbfb8aa3b
	s_mov_b32 s37, 0x3f2aaaab
	s_mov_b32 s28, 0x3f317218
	s_mov_b32 s30, 0xb102e308
	s_mov_b32 s34, 0x3ecc95a3
	s_mov_b32 s36, 0x3e9b6dac
	s_mov_b32 s42, 0x3f2aaada
	s_mov_b32 s43, 0x7f800000
	s_mov_b32 s45, 0x33800000
	s_mov_b32 s44, 0x3d800000
	s_mov_b64 s[62:63], 0x10000
	s_mov_b64 s[64:65], 0x20000
	s_mov_b64 s[66:67], 0x30000
	v_mov_b32_e32 v86, 0x7f800000
	v_mov_b32_e32 v87, 0x7fc00000
	v_mov_b32_e32 v88, 0xff800000
	v_writelane_b32 v254, s71, 1
	s_mov_b32 s70, s72
	s_branch .LBB0_147
